# baseline (speedup 1.0000x reference)
_Z11prep_kernelPKfS0_S0_PDF16_PfPiS0_S1_:
	s_cmpk_lt_u32 s2, 0xc1
	s_mov_b64 s[4:5], -1
	s_cbranch_scc0 .LBB0_51
	s_cmpk_lg_i32 s2, 0xc0
	s_cbranch_scc0 .LBB0_11
	s_cmp_gt_u32 s2, 63
	s_cbranch_scc0 .LBB0_8
	s_load_dwordx4 s[4:7], s[0:1], 0x0
	s_load_dwordx2 s[28:29], s[0:1], 0x20
	s_sub_u32 s3, s2, 64
	v_readfirstlane_b32 s23, v0
	v_and_b32_e32 v1, 31, v0
	v_lshlrev_b32_e32 v226, 4, v1
	v_and_b32_e32 v1, 32, v0
	v_lshlrev_b32_e32 v227, 7, v1
	s_lshr_b32 s23, s23, 6
	s_lshr_b32 s27, s3, 2
	s_and_b32 s30, s3, 3
	s_lshl_b32 s8, s27, 13
	s_lshl_b32 s9, s23, 6
	s_add_u32 s8, s8, s9
	s_lshl_b32 s10, s23, 15
	s_lshl_b32 s9, s30, 9
	s_add_u32 s10, s10, s9
	s_waitcnt lgkmcnt(0)
	s_add_u32 s20, s4, s8
	s_addc_u32 s21, s5, 0
	s_add_u32 s24, s6, s10
	s_addc_u32 s25, s7, 0
	global_load_dwordx4 v[98:101], v227, s[20:21] offset:0
	global_load_dwordx4 v[114:117], v227, s[20:21] offset:512
	global_load_dwordx4 v[130:133], v227, s[20:21] offset:1024
	global_load_dwordx4 v[146:149], v227, s[20:21] offset:1536
	global_load_dwordx4 v[162:165], v227, s[20:21] offset:2048
	global_load_dwordx4 v[178:181], v227, s[20:21] offset:2560
	global_load_dwordx4 v[194:197], v227, s[20:21] offset:3072
	global_load_dwordx4 v[210:213], v227, s[20:21] offset:3584
	global_load_dwordx4 v[34:37], v226, s[24:25]
	global_load_dwordx4 v[38:41], v226, s[24:25] offset:2048
	s_add_u32 s24, s24, 0x1000
	s_addc_u32 s25, s25, 0
	global_load_dwordx4 v[42:45], v226, s[24:25]
	global_load_dwordx4 v[46:49], v226, s[24:25] offset:2048
	s_add_u32 s24, s24, 0x1000
	s_addc_u32 s25, s25, 0
	global_load_dwordx4 v[102:105], v227, s[20:21] offset:16
	global_load_dwordx4 v[118:121], v227, s[20:21] offset:528
	global_load_dwordx4 v[134:137], v227, s[20:21] offset:1040
	global_load_dwordx4 v[150:153], v227, s[20:21] offset:1552
	global_load_dwordx4 v[166:169], v227, s[20:21] offset:2064
	global_load_dwordx4 v[182:185], v227, s[20:21] offset:2576
	global_load_dwordx4 v[198:201], v227, s[20:21] offset:3088
	global_load_dwordx4 v[214:217], v227, s[20:21] offset:3600
	global_load_dwordx4 v[50:53], v226, s[24:25]
	global_load_dwordx4 v[54:57], v226, s[24:25] offset:2048
	s_add_u32 s24, s24, 0x1000
	s_addc_u32 s25, s25, 0
	global_load_dwordx4 v[58:61], v226, s[24:25]
	global_load_dwordx4 v[62:65], v226, s[24:25] offset:2048
	s_add_u32 s24, s24, 0x1000
	s_addc_u32 s25, s25, 0
	global_load_dwordx4 v[106:109], v227, s[20:21] offset:32
	global_load_dwordx4 v[122:125], v227, s[20:21] offset:544
	global_load_dwordx4 v[138:141], v227, s[20:21] offset:1056
	global_load_dwordx4 v[154:157], v227, s[20:21] offset:1568
	global_load_dwordx4 v[170:173], v227, s[20:21] offset:2080
	global_load_dwordx4 v[186:189], v227, s[20:21] offset:2592
	global_load_dwordx4 v[202:205], v227, s[20:21] offset:3104
	global_load_dwordx4 v[218:221], v227, s[20:21] offset:3616
	global_load_dwordx4 v[66:69], v226, s[24:25]
	global_load_dwordx4 v[70:73], v226, s[24:25] offset:2048
	s_add_u32 s24, s24, 0x1000
	s_addc_u32 s25, s25, 0
	global_load_dwordx4 v[74:77], v226, s[24:25]
	global_load_dwordx4 v[78:81], v226, s[24:25] offset:2048
	s_add_u32 s24, s24, 0x1000
	s_addc_u32 s25, s25, 0
	global_load_dwordx4 v[110:113], v227, s[20:21] offset:48
	global_load_dwordx4 v[126:129], v227, s[20:21] offset:560
	global_load_dwordx4 v[142:145], v227, s[20:21] offset:1072
	global_load_dwordx4 v[158:161], v227, s[20:21] offset:1584
	global_load_dwordx4 v[174:177], v227, s[20:21] offset:2096
	global_load_dwordx4 v[190:193], v227, s[20:21] offset:2608
	global_load_dwordx4 v[206:209], v227, s[20:21] offset:3120
	global_load_dwordx4 v[222:225], v227, s[20:21] offset:3632
	global_load_dwordx4 v[82:85], v226, s[24:25]
	global_load_dwordx4 v[86:89], v226, s[24:25] offset:2048
	s_add_u32 s24, s24, 0x1000
	s_addc_u32 s25, s25, 0
	global_load_dwordx4 v[90:93], v226, s[24:25]
	global_load_dwordx4 v[94:97], v226, s[24:25] offset:2048
	v_mov_b64_e32 v[2:3], 0
	v_mov_b64_e32 v[4:5], 0
	v_mov_b64_e32 v[6:7], 0
	v_mov_b64_e32 v[8:9], 0
	v_mov_b64_e32 v[10:11], 0
	v_mov_b64_e32 v[12:13], 0
	v_mov_b64_e32 v[14:15], 0
	v_mov_b64_e32 v[16:17], 0
	v_mov_b64_e32 v[18:19], 0
	v_mov_b64_e32 v[20:21], 0
	v_mov_b64_e32 v[22:23], 0
	v_mov_b64_e32 v[24:25], 0
	v_mov_b64_e32 v[26:27], 0
	v_mov_b64_e32 v[28:29], 0
	v_mov_b64_e32 v[30:31], 0
	v_mov_b64_e32 v[32:33], 0
	s_waitcnt vmcnt(39)
	v_pk_fma_f32 v[2:3], v[98:99], v[34:35], v[2:3] op_sel_hi:[0,1,1]
	v_pk_fma_f32 v[4:5], v[98:99], v[36:37], v[4:5] op_sel_hi:[0,1,1]
	v_pk_fma_f32 v[6:7], v[114:115], v[34:35], v[6:7] op_sel_hi:[0,1,1]
	v_pk_fma_f32 v[8:9], v[114:115], v[36:37], v[8:9] op_sel_hi:[0,1,1]
	v_pk_fma_f32 v[10:11], v[130:131], v[34:35], v[10:11] op_sel_hi:[0,1,1]
	v_pk_fma_f32 v[12:13], v[130:131], v[36:37], v[12:13] op_sel_hi:[0,1,1]
	v_pk_fma_f32 v[14:15], v[146:147], v[34:35], v[14:15] op_sel_hi:[0,1,1]
	v_pk_fma_f32 v[16:17], v[146:147], v[36:37], v[16:17] op_sel_hi:[0,1,1]
	v_pk_fma_f32 v[18:19], v[162:163], v[34:35], v[18:19] op_sel_hi:[0,1,1]
	v_pk_fma_f32 v[20:21], v[162:163], v[36:37], v[20:21] op_sel_hi:[0,1,1]
	v_pk_fma_f32 v[22:23], v[178:179], v[34:35], v[22:23] op_sel_hi:[0,1,1]
	v_pk_fma_f32 v[24:25], v[178:179], v[36:37], v[24:25] op_sel_hi:[0,1,1]
	v_pk_fma_f32 v[26:27], v[194:195], v[34:35], v[26:27] op_sel_hi:[0,1,1]
	v_pk_fma_f32 v[28:29], v[194:195], v[36:37], v[28:29] op_sel_hi:[0,1,1]
	v_pk_fma_f32 v[30:31], v[210:211], v[34:35], v[30:31] op_sel_hi:[0,1,1]
	v_pk_fma_f32 v[32:33], v[210:211], v[36:37], v[32:33] op_sel_hi:[0,1,1]
	s_waitcnt vmcnt(38)
	v_pk_fma_f32 v[2:3], v[98:99], v[38:39], v[2:3] op_sel:[1,0,0]
	v_pk_fma_f32 v[4:5], v[98:99], v[40:41], v[4:5] op_sel:[1,0,0]
	v_pk_fma_f32 v[6:7], v[114:115], v[38:39], v[6:7] op_sel:[1,0,0]
	v_pk_fma_f32 v[8:9], v[114:115], v[40:41], v[8:9] op_sel:[1,0,0]
	v_pk_fma_f32 v[10:11], v[130:131], v[38:39], v[10:11] op_sel:[1,0,0]
	v_pk_fma_f32 v[12:13], v[130:131], v[40:41], v[12:13] op_sel:[1,0,0]
	v_pk_fma_f32 v[14:15], v[146:147], v[38:39], v[14:15] op_sel:[1,0,0]
	v_pk_fma_f32 v[16:17], v[146:147], v[40:41], v[16:17] op_sel:[1,0,0]
	v_pk_fma_f32 v[18:19], v[162:163], v[38:39], v[18:19] op_sel:[1,0,0]
	v_pk_fma_f32 v[20:21], v[162:163], v[40:41], v[20:21] op_sel:[1,0,0]
	v_pk_fma_f32 v[22:23], v[178:179], v[38:39], v[22:23] op_sel:[1,0,0]
	v_pk_fma_f32 v[24:25], v[178:179], v[40:41], v[24:25] op_sel:[1,0,0]
	v_pk_fma_f32 v[26:27], v[194:195], v[38:39], v[26:27] op_sel:[1,0,0]
	v_pk_fma_f32 v[28:29], v[194:195], v[40:41], v[28:29] op_sel:[1,0,0]
	v_pk_fma_f32 v[30:31], v[210:211], v[38:39], v[30:31] op_sel:[1,0,0]
	v_pk_fma_f32 v[32:33], v[210:211], v[40:41], v[32:33] op_sel:[1,0,0]
	s_waitcnt vmcnt(37)
	v_pk_fma_f32 v[2:3], v[100:101], v[42:43], v[2:3] op_sel_hi:[0,1,1]
	v_pk_fma_f32 v[4:5], v[100:101], v[44:45], v[4:5] op_sel_hi:[0,1,1]
	v_pk_fma_f32 v[6:7], v[116:117], v[42:43], v[6:7] op_sel_hi:[0,1,1]
	v_pk_fma_f32 v[8:9], v[116:117], v[44:45], v[8:9] op_sel_hi:[0,1,1]
	v_pk_fma_f32 v[10:11], v[132:133], v[42:43], v[10:11] op_sel_hi:[0,1,1]
	v_pk_fma_f32 v[12:13], v[132:133], v[44:45], v[12:13] op_sel_hi:[0,1,1]
	v_pk_fma_f32 v[14:15], v[148:149], v[42:43], v[14:15] op_sel_hi:[0,1,1]
	v_pk_fma_f32 v[16:17], v[148:149], v[44:45], v[16:17] op_sel_hi:[0,1,1]
	v_pk_fma_f32 v[18:19], v[164:165], v[42:43], v[18:19] op_sel_hi:[0,1,1]
	v_pk_fma_f32 v[20:21], v[164:165], v[44:45], v[20:21] op_sel_hi:[0,1,1]
	v_pk_fma_f32 v[22:23], v[180:181], v[42:43], v[22:23] op_sel_hi:[0,1,1]
	v_pk_fma_f32 v[24:25], v[180:181], v[44:45], v[24:25] op_sel_hi:[0,1,1]
	v_pk_fma_f32 v[26:27], v[196:197], v[42:43], v[26:27] op_sel_hi:[0,1,1]
	v_pk_fma_f32 v[28:29], v[196:197], v[44:45], v[28:29] op_sel_hi:[0,1,1]
	v_pk_fma_f32 v[30:31], v[212:213], v[42:43], v[30:31] op_sel_hi:[0,1,1]
	v_pk_fma_f32 v[32:33], v[212:213], v[44:45], v[32:33] op_sel_hi:[0,1,1]
	s_waitcnt vmcnt(36)
	v_pk_fma_f32 v[2:3], v[100:101], v[46:47], v[2:3] op_sel:[1,0,0]
	v_pk_fma_f32 v[4:5], v[100:101], v[48:49], v[4:5] op_sel:[1,0,0]
	v_pk_fma_f32 v[6:7], v[116:117], v[46:47], v[6:7] op_sel:[1,0,0]
	v_pk_fma_f32 v[8:9], v[116:117], v[48:49], v[8:9] op_sel:[1,0,0]
	v_pk_fma_f32 v[10:11], v[132:133], v[46:47], v[10:11] op_sel:[1,0,0]
	v_pk_fma_f32 v[12:13], v[132:133], v[48:49], v[12:13] op_sel:[1,0,0]
	v_pk_fma_f32 v[14:15], v[148:149], v[46:47], v[14:15] op_sel:[1,0,0]
	v_pk_fma_f32 v[16:17], v[148:149], v[48:49], v[16:17] op_sel:[1,0,0]
	v_pk_fma_f32 v[18:19], v[164:165], v[46:47], v[18:19] op_sel:[1,0,0]
	v_pk_fma_f32 v[20:21], v[164:165], v[48:49], v[20:21] op_sel:[1,0,0]
	v_pk_fma_f32 v[22:23], v[180:181], v[46:47], v[22:23] op_sel:[1,0,0]
	v_pk_fma_f32 v[24:25], v[180:181], v[48:49], v[24:25] op_sel:[1,0,0]
	v_pk_fma_f32 v[26:27], v[196:197], v[46:47], v[26:27] op_sel:[1,0,0]
	v_pk_fma_f32 v[28:29], v[196:197], v[48:49], v[28:29] op_sel:[1,0,0]
	v_pk_fma_f32 v[30:31], v[212:213], v[46:47], v[30:31] op_sel:[1,0,0]
	v_pk_fma_f32 v[32:33], v[212:213], v[48:49], v[32:33] op_sel:[1,0,0]
	s_waitcnt vmcnt(27)
	v_pk_fma_f32 v[2:3], v[102:103], v[50:51], v[2:3] op_sel_hi:[0,1,1]
	v_pk_fma_f32 v[4:5], v[102:103], v[52:53], v[4:5] op_sel_hi:[0,1,1]
	v_pk_fma_f32 v[6:7], v[118:119], v[50:51], v[6:7] op_sel_hi:[0,1,1]
	v_pk_fma_f32 v[8:9], v[118:119], v[52:53], v[8:9] op_sel_hi:[0,1,1]
	v_pk_fma_f32 v[10:11], v[134:135], v[50:51], v[10:11] op_sel_hi:[0,1,1]
	v_pk_fma_f32 v[12:13], v[134:135], v[52:53], v[12:13] op_sel_hi:[0,1,1]
	v_pk_fma_f32 v[14:15], v[150:151], v[50:51], v[14:15] op_sel_hi:[0,1,1]
	v_pk_fma_f32 v[16:17], v[150:151], v[52:53], v[16:17] op_sel_hi:[0,1,1]
	v_pk_fma_f32 v[18:19], v[166:167], v[50:51], v[18:19] op_sel_hi:[0,1,1]
	v_pk_fma_f32 v[20:21], v[166:167], v[52:53], v[20:21] op_sel_hi:[0,1,1]
	v_pk_fma_f32 v[22:23], v[182:183], v[50:51], v[22:23] op_sel_hi:[0,1,1]
	v_pk_fma_f32 v[24:25], v[182:183], v[52:53], v[24:25] op_sel_hi:[0,1,1]
	v_pk_fma_f32 v[26:27], v[198:199], v[50:51], v[26:27] op_sel_hi:[0,1,1]
	v_pk_fma_f32 v[28:29], v[198:199], v[52:53], v[28:29] op_sel_hi:[0,1,1]
	v_pk_fma_f32 v[30:31], v[214:215], v[50:51], v[30:31] op_sel_hi:[0,1,1]
	v_pk_fma_f32 v[32:33], v[214:215], v[52:53], v[32:33] op_sel_hi:[0,1,1]
	s_waitcnt vmcnt(26)
	v_pk_fma_f32 v[2:3], v[102:103], v[54:55], v[2:3] op_sel:[1,0,0]
	v_pk_fma_f32 v[4:5], v[102:103], v[56:57], v[4:5] op_sel:[1,0,0]
	v_pk_fma_f32 v[6:7], v[118:119], v[54:55], v[6:7] op_sel:[1,0,0]
	v_pk_fma_f32 v[8:9], v[118:119], v[56:57], v[8:9] op_sel:[1,0,0]
	v_pk_fma_f32 v[10:11], v[134:135], v[54:55], v[10:11] op_sel:[1,0,0]
	v_pk_fma_f32 v[12:13], v[134:135], v[56:57], v[12:13] op_sel:[1,0,0]
	v_pk_fma_f32 v[14:15], v[150:151], v[54:55], v[14:15] op_sel:[1,0,0]
	v_pk_fma_f32 v[16:17], v[150:151], v[56:57], v[16:17] op_sel:[1,0,0]
	v_pk_fma_f32 v[18:19], v[166:167], v[54:55], v[18:19] op_sel:[1,0,0]
	v_pk_fma_f32 v[20:21], v[166:167], v[56:57], v[20:21] op_sel:[1,0,0]
	v_pk_fma_f32 v[22:23], v[182:183], v[54:55], v[22:23] op_sel:[1,0,0]
	v_pk_fma_f32 v[24:25], v[182:183], v[56:57], v[24:25] op_sel:[1,0,0]
	v_pk_fma_f32 v[26:27], v[198:199], v[54:55], v[26:27] op_sel:[1,0,0]
	v_pk_fma_f32 v[28:29], v[198:199], v[56:57], v[28:29] op_sel:[1,0,0]
	v_pk_fma_f32 v[30:31], v[214:215], v[54:55], v[30:31] op_sel:[1,0,0]
	v_pk_fma_f32 v[32:33], v[214:215], v[56:57], v[32:33] op_sel:[1,0,0]
	s_waitcnt vmcnt(25)
	v_pk_fma_f32 v[2:3], v[104:105], v[58:59], v[2:3] op_sel_hi:[0,1,1]
	v_pk_fma_f32 v[4:5], v[104:105], v[60:61], v[4:5] op_sel_hi:[0,1,1]
	v_pk_fma_f32 v[6:7], v[120:121], v[58:59], v[6:7] op_sel_hi:[0,1,1]
	v_pk_fma_f32 v[8:9], v[120:121], v[60:61], v[8:9] op_sel_hi:[0,1,1]
	v_pk_fma_f32 v[10:11], v[136:137], v[58:59], v[10:11] op_sel_hi:[0,1,1]
	v_pk_fma_f32 v[12:13], v[136:137], v[60:61], v[12:13] op_sel_hi:[0,1,1]
	v_pk_fma_f32 v[14:15], v[152:153], v[58:59], v[14:15] op_sel_hi:[0,1,1]
	v_pk_fma_f32 v[16:17], v[152:153], v[60:61], v[16:17] op_sel_hi:[0,1,1]
	v_pk_fma_f32 v[18:19], v[168:169], v[58:59], v[18:19] op_sel_hi:[0,1,1]
	v_pk_fma_f32 v[20:21], v[168:169], v[60:61], v[20:21] op_sel_hi:[0,1,1]
	v_pk_fma_f32 v[22:23], v[184:185], v[58:59], v[22:23] op_sel_hi:[0,1,1]
	v_pk_fma_f32 v[24:25], v[184:185], v[60:61], v[24:25] op_sel_hi:[0,1,1]
	v_pk_fma_f32 v[26:27], v[200:201], v[58:59], v[26:27] op_sel_hi:[0,1,1]
	v_pk_fma_f32 v[28:29], v[200:201], v[60:61], v[28:29] op_sel_hi:[0,1,1]
	v_pk_fma_f32 v[30:31], v[216:217], v[58:59], v[30:31] op_sel_hi:[0,1,1]
	v_pk_fma_f32 v[32:33], v[216:217], v[60:61], v[32:33] op_sel_hi:[0,1,1]
	s_waitcnt vmcnt(24)
	v_pk_fma_f32 v[2:3], v[104:105], v[62:63], v[2:3] op_sel:[1,0,0]
	v_pk_fma_f32 v[4:5], v[104:105], v[64:65], v[4:5] op_sel:[1,0,0]
	v_pk_fma_f32 v[6:7], v[120:121], v[62:63], v[6:7] op_sel:[1,0,0]
	v_pk_fma_f32 v[8:9], v[120:121], v[64:65], v[8:9] op_sel:[1,0,0]
	v_pk_fma_f32 v[10:11], v[136:137], v[62:63], v[10:11] op_sel:[1,0,0]
	v_pk_fma_f32 v[12:13], v[136:137], v[64:65], v[12:13] op_sel:[1,0,0]
	v_pk_fma_f32 v[14:15], v[152:153], v[62:63], v[14:15] op_sel:[1,0,0]
	v_pk_fma_f32 v[16:17], v[152:153], v[64:65], v[16:17] op_sel:[1,0,0]
	v_pk_fma_f32 v[18:19], v[168:169], v[62:63], v[18:19] op_sel:[1,0,0]
	v_pk_fma_f32 v[20:21], v[168:169], v[64:65], v[20:21] op_sel:[1,0,0]
	v_pk_fma_f32 v[22:23], v[184:185], v[62:63], v[22:23] op_sel:[1,0,0]
	v_pk_fma_f32 v[24:25], v[184:185], v[64:65], v[24:25] op_sel:[1,0,0]
	v_pk_fma_f32 v[26:27], v[200:201], v[62:63], v[26:27] op_sel:[1,0,0]
	v_pk_fma_f32 v[28:29], v[200:201], v[64:65], v[28:29] op_sel:[1,0,0]
	v_pk_fma_f32 v[30:31], v[216:217], v[62:63], v[30:31] op_sel:[1,0,0]
	v_pk_fma_f32 v[32:33], v[216:217], v[64:65], v[32:33] op_sel:[1,0,0]
	s_waitcnt vmcnt(15)
	v_pk_fma_f32 v[2:3], v[106:107], v[66:67], v[2:3] op_sel_hi:[0,1,1]
	v_pk_fma_f32 v[4:5], v[106:107], v[68:69], v[4:5] op_sel_hi:[0,1,1]
	v_pk_fma_f32 v[6:7], v[122:123], v[66:67], v[6:7] op_sel_hi:[0,1,1]
	v_pk_fma_f32 v[8:9], v[122:123], v[68:69], v[8:9] op_sel_hi:[0,1,1]
	v_pk_fma_f32 v[10:11], v[138:139], v[66:67], v[10:11] op_sel_hi:[0,1,1]
	v_pk_fma_f32 v[12:13], v[138:139], v[68:69], v[12:13] op_sel_hi:[0,1,1]
	v_pk_fma_f32 v[14:15], v[154:155], v[66:67], v[14:15] op_sel_hi:[0,1,1]
	v_pk_fma_f32 v[16:17], v[154:155], v[68:69], v[16:17] op_sel_hi:[0,1,1]
	v_pk_fma_f32 v[18:19], v[170:171], v[66:67], v[18:19] op_sel_hi:[0,1,1]
	v_pk_fma_f32 v[20:21], v[170:171], v[68:69], v[20:21] op_sel_hi:[0,1,1]
	v_pk_fma_f32 v[22:23], v[186:187], v[66:67], v[22:23] op_sel_hi:[0,1,1]
	v_pk_fma_f32 v[24:25], v[186:187], v[68:69], v[24:25] op_sel_hi:[0,1,1]
	v_pk_fma_f32 v[26:27], v[202:203], v[66:67], v[26:27] op_sel_hi:[0,1,1]
	v_pk_fma_f32 v[28:29], v[202:203], v[68:69], v[28:29] op_sel_hi:[0,1,1]
	v_pk_fma_f32 v[30:31], v[218:219], v[66:67], v[30:31] op_sel_hi:[0,1,1]
	v_pk_fma_f32 v[32:33], v[218:219], v[68:69], v[32:33] op_sel_hi:[0,1,1]
	s_waitcnt vmcnt(14)
	v_pk_fma_f32 v[2:3], v[106:107], v[70:71], v[2:3] op_sel:[1,0,0]
	v_pk_fma_f32 v[4:5], v[106:107], v[72:73], v[4:5] op_sel:[1,0,0]
	v_pk_fma_f32 v[6:7], v[122:123], v[70:71], v[6:7] op_sel:[1,0,0]
	v_pk_fma_f32 v[8:9], v[122:123], v[72:73], v[8:9] op_sel:[1,0,0]
	v_pk_fma_f32 v[10:11], v[138:139], v[70:71], v[10:11] op_sel:[1,0,0]
	v_pk_fma_f32 v[12:13], v[138:139], v[72:73], v[12:13] op_sel:[1,0,0]
	v_pk_fma_f32 v[14:15], v[154:155], v[70:71], v[14:15] op_sel:[1,0,0]
	v_pk_fma_f32 v[16:17], v[154:155], v[72:73], v[16:17] op_sel:[1,0,0]
	v_pk_fma_f32 v[18:19], v[170:171], v[70:71], v[18:19] op_sel:[1,0,0]
	v_pk_fma_f32 v[20:21], v[170:171], v[72:73], v[20:21] op_sel:[1,0,0]
	v_pk_fma_f32 v[22:23], v[186:187], v[70:71], v[22:23] op_sel:[1,0,0]
	v_pk_fma_f32 v[24:25], v[186:187], v[72:73], v[24:25] op_sel:[1,0,0]
	v_pk_fma_f32 v[26:27], v[202:203], v[70:71], v[26:27] op_sel:[1,0,0]
	v_pk_fma_f32 v[28:29], v[202:203], v[72:73], v[28:29] op_sel:[1,0,0]
	v_pk_fma_f32 v[30:31], v[218:219], v[70:71], v[30:31] op_sel:[1,0,0]
	v_pk_fma_f32 v[32:33], v[218:219], v[72:73], v[32:33] op_sel:[1,0,0]
	s_waitcnt vmcnt(13)
	v_pk_fma_f32 v[2:3], v[108:109], v[74:75], v[2:3] op_sel_hi:[0,1,1]
	v_pk_fma_f32 v[4:5], v[108:109], v[76:77], v[4:5] op_sel_hi:[0,1,1]
	v_pk_fma_f32 v[6:7], v[124:125], v[74:75], v[6:7] op_sel_hi:[0,1,1]
	v_pk_fma_f32 v[8:9], v[124:125], v[76:77], v[8:9] op_sel_hi:[0,1,1]
	v_pk_fma_f32 v[10:11], v[140:141], v[74:75], v[10:11] op_sel_hi:[0,1,1]
	v_pk_fma_f32 v[12:13], v[140:141], v[76:77], v[12:13] op_sel_hi:[0,1,1]
	v_pk_fma_f32 v[14:15], v[156:157], v[74:75], v[14:15] op_sel_hi:[0,1,1]
	v_pk_fma_f32 v[16:17], v[156:157], v[76:77], v[16:17] op_sel_hi:[0,1,1]
	v_pk_fma_f32 v[18:19], v[172:173], v[74:75], v[18:19] op_sel_hi:[0,1,1]
	v_pk_fma_f32 v[20:21], v[172:173], v[76:77], v[20:21] op_sel_hi:[0,1,1]
	v_pk_fma_f32 v[22:23], v[188:189], v[74:75], v[22:23] op_sel_hi:[0,1,1]
	v_pk_fma_f32 v[24:25], v[188:189], v[76:77], v[24:25] op_sel_hi:[0,1,1]
	v_pk_fma_f32 v[26:27], v[204:205], v[74:75], v[26:27] op_sel_hi:[0,1,1]
	v_pk_fma_f32 v[28:29], v[204:205], v[76:77], v[28:29] op_sel_hi:[0,1,1]
	v_pk_fma_f32 v[30:31], v[220:221], v[74:75], v[30:31] op_sel_hi:[0,1,1]
	v_pk_fma_f32 v[32:33], v[220:221], v[76:77], v[32:33] op_sel_hi:[0,1,1]
	s_waitcnt vmcnt(12)
	v_pk_fma_f32 v[2:3], v[108:109], v[78:79], v[2:3] op_sel:[1,0,0]
	v_pk_fma_f32 v[4:5], v[108:109], v[80:81], v[4:5] op_sel:[1,0,0]
	v_pk_fma_f32 v[6:7], v[124:125], v[78:79], v[6:7] op_sel:[1,0,0]
	v_pk_fma_f32 v[8:9], v[124:125], v[80:81], v[8:9] op_sel:[1,0,0]
	v_pk_fma_f32 v[10:11], v[140:141], v[78:79], v[10:11] op_sel:[1,0,0]
	v_pk_fma_f32 v[12:13], v[140:141], v[80:81], v[12:13] op_sel:[1,0,0]
	v_pk_fma_f32 v[14:15], v[156:157], v[78:79], v[14:15] op_sel:[1,0,0]
	v_pk_fma_f32 v[16:17], v[156:157], v[80:81], v[16:17] op_sel:[1,0,0]
	v_pk_fma_f32 v[18:19], v[172:173], v[78:79], v[18:19] op_sel:[1,0,0]
	v_pk_fma_f32 v[20:21], v[172:173], v[80:81], v[20:21] op_sel:[1,0,0]
	v_pk_fma_f32 v[22:23], v[188:189], v[78:79], v[22:23] op_sel:[1,0,0]
	v_pk_fma_f32 v[24:25], v[188:189], v[80:81], v[24:25] op_sel:[1,0,0]
	v_pk_fma_f32 v[26:27], v[204:205], v[78:79], v[26:27] op_sel:[1,0,0]
	v_pk_fma_f32 v[28:29], v[204:205], v[80:81], v[28:29] op_sel:[1,0,0]
	v_pk_fma_f32 v[30:31], v[220:221], v[78:79], v[30:31] op_sel:[1,0,0]
	v_pk_fma_f32 v[32:33], v[220:221], v[80:81], v[32:33] op_sel:[1,0,0]
	s_waitcnt vmcnt(3)
	v_pk_fma_f32 v[2:3], v[110:111], v[82:83], v[2:3] op_sel_hi:[0,1,1]
	v_pk_fma_f32 v[4:5], v[110:111], v[84:85], v[4:5] op_sel_hi:[0,1,1]
	v_pk_fma_f32 v[6:7], v[126:127], v[82:83], v[6:7] op_sel_hi:[0,1,1]
	v_pk_fma_f32 v[8:9], v[126:127], v[84:85], v[8:9] op_sel_hi:[0,1,1]
	v_pk_fma_f32 v[10:11], v[142:143], v[82:83], v[10:11] op_sel_hi:[0,1,1]
	v_pk_fma_f32 v[12:13], v[142:143], v[84:85], v[12:13] op_sel_hi:[0,1,1]
	v_pk_fma_f32 v[14:15], v[158:159], v[82:83], v[14:15] op_sel_hi:[0,1,1]
	v_pk_fma_f32 v[16:17], v[158:159], v[84:85], v[16:17] op_sel_hi:[0,1,1]
	v_pk_fma_f32 v[18:19], v[174:175], v[82:83], v[18:19] op_sel_hi:[0,1,1]
	v_pk_fma_f32 v[20:21], v[174:175], v[84:85], v[20:21] op_sel_hi:[0,1,1]
	v_pk_fma_f32 v[22:23], v[190:191], v[82:83], v[22:23] op_sel_hi:[0,1,1]
	v_pk_fma_f32 v[24:25], v[190:191], v[84:85], v[24:25] op_sel_hi:[0,1,1]
	v_pk_fma_f32 v[26:27], v[206:207], v[82:83], v[26:27] op_sel_hi:[0,1,1]
	v_pk_fma_f32 v[28:29], v[206:207], v[84:85], v[28:29] op_sel_hi:[0,1,1]
	v_pk_fma_f32 v[30:31], v[222:223], v[82:83], v[30:31] op_sel_hi:[0,1,1]
	v_pk_fma_f32 v[32:33], v[222:223], v[84:85], v[32:33] op_sel_hi:[0,1,1]
	s_waitcnt vmcnt(2)
	v_pk_fma_f32 v[2:3], v[110:111], v[86:87], v[2:3] op_sel:[1,0,0]
	v_pk_fma_f32 v[4:5], v[110:111], v[88:89], v[4:5] op_sel:[1,0,0]
	v_pk_fma_f32 v[6:7], v[126:127], v[86:87], v[6:7] op_sel:[1,0,0]
	v_pk_fma_f32 v[8:9], v[126:127], v[88:89], v[8:9] op_sel:[1,0,0]
	v_pk_fma_f32 v[10:11], v[142:143], v[86:87], v[10:11] op_sel:[1,0,0]
	v_pk_fma_f32 v[12:13], v[142:143], v[88:89], v[12:13] op_sel:[1,0,0]
	v_pk_fma_f32 v[14:15], v[158:159], v[86:87], v[14:15] op_sel:[1,0,0]
	v_pk_fma_f32 v[16:17], v[158:159], v[88:89], v[16:17] op_sel:[1,0,0]
	v_pk_fma_f32 v[18:19], v[174:175], v[86:87], v[18:19] op_sel:[1,0,0]
	v_pk_fma_f32 v[20:21], v[174:175], v[88:89], v[20:21] op_sel:[1,0,0]
	v_pk_fma_f32 v[22:23], v[190:191], v[86:87], v[22:23] op_sel:[1,0,0]
	v_pk_fma_f32 v[24:25], v[190:191], v[88:89], v[24:25] op_sel:[1,0,0]
	v_pk_fma_f32 v[26:27], v[206:207], v[86:87], v[26:27] op_sel:[1,0,0]
	v_pk_fma_f32 v[28:29], v[206:207], v[88:89], v[28:29] op_sel:[1,0,0]
	v_pk_fma_f32 v[30:31], v[222:223], v[86:87], v[30:31] op_sel:[1,0,0]
	v_pk_fma_f32 v[32:33], v[222:223], v[88:89], v[32:33] op_sel:[1,0,0]
	s_waitcnt vmcnt(1)
	v_pk_fma_f32 v[2:3], v[112:113], v[90:91], v[2:3] op_sel_hi:[0,1,1]
	v_pk_fma_f32 v[4:5], v[112:113], v[92:93], v[4:5] op_sel_hi:[0,1,1]
	v_pk_fma_f32 v[6:7], v[128:129], v[90:91], v[6:7] op_sel_hi:[0,1,1]
	v_pk_fma_f32 v[8:9], v[128:129], v[92:93], v[8:9] op_sel_hi:[0,1,1]
	v_pk_fma_f32 v[10:11], v[144:145], v[90:91], v[10:11] op_sel_hi:[0,1,1]
	v_pk_fma_f32 v[12:13], v[144:145], v[92:93], v[12:13] op_sel_hi:[0,1,1]
	v_pk_fma_f32 v[14:15], v[160:161], v[90:91], v[14:15] op_sel_hi:[0,1,1]
	v_pk_fma_f32 v[16:17], v[160:161], v[92:93], v[16:17] op_sel_hi:[0,1,1]
	v_pk_fma_f32 v[18:19], v[176:177], v[90:91], v[18:19] op_sel_hi:[0,1,1]
	v_pk_fma_f32 v[20:21], v[176:177], v[92:93], v[20:21] op_sel_hi:[0,1,1]
	v_pk_fma_f32 v[22:23], v[192:193], v[90:91], v[22:23] op_sel_hi:[0,1,1]
	v_pk_fma_f32 v[24:25], v[192:193], v[92:93], v[24:25] op_sel_hi:[0,1,1]
	v_pk_fma_f32 v[26:27], v[208:209], v[90:91], v[26:27] op_sel_hi:[0,1,1]
	v_pk_fma_f32 v[28:29], v[208:209], v[92:93], v[28:29] op_sel_hi:[0,1,1]
	v_pk_fma_f32 v[30:31], v[224:225], v[90:91], v[30:31] op_sel_hi:[0,1,1]
	v_pk_fma_f32 v[32:33], v[224:225], v[92:93], v[32:33] op_sel_hi:[0,1,1]
	s_waitcnt vmcnt(0)
	v_pk_fma_f32 v[2:3], v[112:113], v[94:95], v[2:3] op_sel:[1,0,0]
	v_pk_fma_f32 v[4:5], v[112:113], v[96:97], v[4:5] op_sel:[1,0,0]
	v_pk_fma_f32 v[6:7], v[128:129], v[94:95], v[6:7] op_sel:[1,0,0]
	v_pk_fma_f32 v[8:9], v[128:129], v[96:97], v[8:9] op_sel:[1,0,0]
	v_pk_fma_f32 v[10:11], v[144:145], v[94:95], v[10:11] op_sel:[1,0,0]
	v_pk_fma_f32 v[12:13], v[144:145], v[96:97], v[12:13] op_sel:[1,0,0]
	v_pk_fma_f32 v[14:15], v[160:161], v[94:95], v[14:15] op_sel:[1,0,0]
	v_pk_fma_f32 v[16:17], v[160:161], v[96:97], v[16:17] op_sel:[1,0,0]
	v_pk_fma_f32 v[18:19], v[176:177], v[94:95], v[18:19] op_sel:[1,0,0]
	v_pk_fma_f32 v[20:21], v[176:177], v[96:97], v[20:21] op_sel:[1,0,0]
	v_pk_fma_f32 v[22:23], v[192:193], v[94:95], v[22:23] op_sel:[1,0,0]
	v_pk_fma_f32 v[24:25], v[192:193], v[96:97], v[24:25] op_sel:[1,0,0]
	v_pk_fma_f32 v[26:27], v[208:209], v[94:95], v[26:27] op_sel:[1,0,0]
	v_pk_fma_f32 v[28:29], v[208:209], v[96:97], v[28:29] op_sel:[1,0,0]
	v_pk_fma_f32 v[30:31], v[224:225], v[94:95], v[30:31] op_sel:[1,0,0]
	v_pk_fma_f32 v[32:33], v[224:225], v[96:97], v[32:33] op_sel:[1,0,0]
	s_lshl_b32 s9, s23, 13
	v_add3_u32 v228, v226, v227, s9
	ds_write_b128 v228, v[2:5] offset:0
	ds_write_b128 v228, v[6:9] offset:512
	ds_write_b128 v228, v[10:13] offset:1024
	ds_write_b128 v228, v[14:17] offset:1536
	ds_write_b128 v228, v[18:21] offset:2048
	ds_write_b128 v228, v[22:25] offset:2560
	ds_write_b128 v228, v[26:29] offset:3072
	ds_write_b128 v228, v[30:33] offset:3584
	v_lshrrev_b32_e32 v229, 3, v227
	s_lshl_b32 s9, s23, 10
	v_add3_u32 v229, v229, v226, s9
	s_waitcnt lgkmcnt(0)
	s_barrier
	ds_read_b128 v[34:37], v229 offset:0
	ds_read_b128 v[38:41], v229 offset:8192
	ds_read_b128 v[42:45], v229 offset:16384
	ds_read_b128 v[46:49], v229 offset:24576
	ds_read_b128 v[50:53], v229 offset:32768
	ds_read_b128 v[54:57], v229 offset:40960
	ds_read_b128 v[58:61], v229 offset:49152
	ds_read_b128 v[62:65], v229 offset:57344
	s_lshl_b32 s8, s27, 4
	s_lshl_b32 s9, s23, 1
	s_add_u32 s8, s8, s9
	s_lshl_b32 s8, s8, 11
	s_lshl_b32 s9, s30, 9
	s_add_u32 s8, s8, s9
	s_add_u32 s28, s28, s8
	s_addc_u32 s29, s29, 0
	v_lshrrev_b32_e32 v228, 1, v227
	v_add_u32_e32 v228, v228, v226
	s_waitcnt lgkmcnt(6)
	v_pk_add_f32 v[34:35], v[34:35], v[38:39]
	v_pk_add_f32 v[36:37], v[36:37], v[40:41]
	s_waitcnt lgkmcnt(5)
	v_pk_add_f32 v[34:35], v[34:35], v[42:43]
	v_pk_add_f32 v[36:37], v[36:37], v[44:45]
	s_waitcnt lgkmcnt(4)
	v_pk_add_f32 v[34:35], v[34:35], v[46:47]
	v_pk_add_f32 v[36:37], v[36:37], v[48:49]
	s_waitcnt lgkmcnt(3)
	v_pk_add_f32 v[34:35], v[34:35], v[50:51]
	v_pk_add_f32 v[36:37], v[36:37], v[52:53]
	s_waitcnt lgkmcnt(2)
	v_pk_add_f32 v[34:35], v[34:35], v[54:55]
	v_pk_add_f32 v[36:37], v[36:37], v[56:57]
	s_waitcnt lgkmcnt(1)
	v_pk_add_f32 v[34:35], v[34:35], v[58:59]
	v_pk_add_f32 v[36:37], v[36:37], v[60:61]
	s_waitcnt lgkmcnt(0)
	v_pk_add_f32 v[34:35], v[34:35], v[62:63]
	v_pk_add_f32 v[36:37], v[36:37], v[64:65]
	global_store_dwordx4 v228, v[34:37], s[28:29]

	.amdhsa_kernel _Z11prep_kernelPKfS0_S0_PDF16_PfPiS0_S1_
		.amdhsa_group_segment_fixed_size 65536
		.amdhsa_private_segment_fixed_size 0
		.amdhsa_kernarg_size 64
		.amdhsa_user_sgpr_count 2
		.amdhsa_user_sgpr_dispatch_ptr 0
		.amdhsa_user_sgpr_queue_ptr 0
		.amdhsa_user_sgpr_kernarg_segment_ptr 1
		.amdhsa_user_sgpr_dispatch_id 0
		.amdhsa_user_sgpr_kernarg_preload_length 0
		.amdhsa_user_sgpr_kernarg_preload_offset 0
		.amdhsa_user_sgpr_private_segment_size 0
		.amdhsa_uses_dynamic_stack 0
		.amdhsa_enable_private_segment 0
		.amdhsa_system_sgpr_workgroup_id_x 1
		.amdhsa_system_sgpr_workgroup_id_y 0
		.amdhsa_system_sgpr_workgroup_id_z 0
		.amdhsa_system_sgpr_workgroup_info 0
		.amdhsa_system_vgpr_workitem_id 0
		.amdhsa_next_free_vgpr 232
		.amdhsa_next_free_sgpr 96
		.amdhsa_accum_offset 232
		.amdhsa_reserve_vcc 1
		.amdhsa_float_round_mode_32 0
		.amdhsa_float_round_mode_16_64 0
		.amdhsa_float_denorm_mode_32 3
		.amdhsa_float_denorm_mode_16_64 3
		.amdhsa_dx10_clamp 1
		.amdhsa_ieee_mode 1
		.amdhsa_fp16_overflow 0
		.amdhsa_tg_split 0
		.amdhsa_exception_fp_ieee_invalid_op 0
		.amdhsa_exception_fp_denorm_src 0
		.amdhsa_exception_fp_ieee_div_zero 0
		.amdhsa_exception_fp_ieee_overflow 0
		.amdhsa_exception_fp_ieee_underflow 0
		.amdhsa_exception_fp_ieee_inexact 0
		.amdhsa_exception_int_div_zero 0
	.end_amdhsa_kernel

amdhsa.kernels:
  - .agpr_count:     0
    .args:
      - .actual_access:  read_only
        .address_space:  global
        .offset:         0
        .size:           8
        .value_kind:     global_buffer
      - .actual_access:  read_only
        .address_space:  global
        .offset:         8
        .size:           8
        .value_kind:     global_buffer
      - .actual_access:  read_only
        .address_space:  global
        .offset:         16
        .size:           8
        .value_kind:     global_buffer
      - .actual_access:  write_only
        .address_space:  global
        .offset:         24
        .size:           8
        .value_kind:     global_buffer
      - .actual_access:  write_only
        .address_space:  global
        .offset:         32
        .size:           8
        .value_kind:     global_buffer
      - .actual_access:  write_only
        .address_space:  global
        .offset:         40
        .size:           8
        .value_kind:     global_buffer
      - .actual_access:  read_only
        .address_space:  global
        .offset:         48
        .size:           8
        .value_kind:     global_buffer
      - .actual_access:  write_only
        .address_space:  global
        .offset:         56
        .size:           8
        .value_kind:     global_buffer
    .group_segment_fixed_size: 65536
    .kernarg_segment_align: 8
    .kernarg_segment_size: 64
    .language:       OpenCL C
    .language_version:
      - 2
      - 0
    .max_flat_workgroup_size: 512
    .name:           _Z11prep_kernelPKfS0_S0_PDF16_PfPiS0_S1_
    .private_segment_fixed_size: 0
    .sgpr_count:     102
    .sgpr_spill_count: 0
    .symbol:         _Z11prep_kernelPKfS0_S0_PDF16_PfPiS0_S1_.kd
    .uniform_work_group_size: 1
    .uses_dynamic_stack: false
    .vgpr_count:     232
    .vgpr_spill_count: 0
    .wavefront_size: 64
  - .agpr_count:     256
    .args:
      - .actual_access:  read_only
        .address_space:  global
        .offset:         0
        .size:           8
        .value_kind:     global_buffer
      - .actual_access:  read_only
        .address_space:  global
        .offset:         8
        .size:           8
        .value_kind:     global_buffer
      - .actual_access:  read_only
        .address_space:  global
        .offset:         16
        .size:           8
        .value_kind:     global_buffer
      - .actual_access:  write_only
        .address_space:  global
        .offset:         24
        .size:           8
        .value_kind:     global_buffer
      - .actual_access:  read_only
        .address_space:  global
        .offset:         32
        .size:           8
        .value_kind:     global_buffer
    .group_segment_fixed_size: 148624
    .kernarg_segment_align: 8
    .kernarg_segment_size: 40
    .language:       OpenCL C
    .language_version:
      - 2
      - 0
    .max_flat_workgroup_size: 256
    .name:           _Z10ode_kernelPKfPKDF16_S2_PfPKi
    .private_segment_fixed_size: 0
    .sgpr_count:     59
    .sgpr_spill_count: 0
    .symbol:         _Z10ode_kernelPKfPKDF16_S2_PfPKi.kd
    .uniform_work_group_size: 1
    .uses_dynamic_stack: false
    .vgpr_count:     512
    .vgpr_spill_count: 0
    .wavefront_size: 64
